# static s_setprio 1 for waves 4-7 from the start of each sparse-attention unit (lever: one static priority raise for the younger half)
# baseline (speedup 1.0000x reference)
; #define LAS __attribute__((address_space(3)))
; __device__ __forceinline__ void dsa2_unit(LAS unsigned char* lds, const bf16* PROJ, const bf16* KIDX, const bf16* KVN, bf16* OLAT, float* sbuf, int b, int t0, int tid) {
;     ...
;     const int lane = tid & 63, wave = __builtin_amdgcn_readfirstlane(tid >> 6), r = lane & 31, h = lane >> 5;
;     const size_t rowb = (size_t)b * T;
;     LAS unsigned char* wl = lds + wave * 16384; LAS unsigned* hist = (LAS unsigned*)wl; LAS int* LIST = (LAS int*)(wl + 12288);
;     const int t = t0 + wave; int cnt;
;     ...
;     } else {
; #pragma unroll
;         for (int j = 0; j < 4; ++j) LIST[lane + 64 * j] = lane + 64 * j;
;         cnt = t + 1;
; __global__ void __launch_bounds__(NWAVES * 64, 2) fwd(Args args) {
;     ...
;                 const int u = M / 8 - 1 - rk; const int b = u & 1, t0 = (u >> 1) * 8;
;                 dsa2_unit(F.lds, PROJ, KIDX, KVN, OLAT, sb0 + (size_t)par * 8 * 8192, b, t0, F.tid); if (t0 >= 256) par ^= 1; }
.LBB0_699:
	s_mov_b64 s[2:3], 0
	s_and_b64 vcc, exec, s[0:1]
	s_cbranch_vccz .LBB0_685
	s_cmpk_gt_i32 s4, 0x7ff
	s_cbranch_scc1 .LBB0_685
	s_sub_i32 s1, 0x7ff, s4
	s_lshl_b32 s0, s1, 2
	v_mov_b32_e32 v150, v156
	s_and_b32 s4, s0, 0x7ffffff8
	s_mov_b64 s[2:3], -1
	v_readfirstlane_b32 s0, v150
	s_ashr_i32 s0, s0, 6
	s_cmp_lt_u32 s0, 4
	s_cbranch_scc1 .Lprio_skip
	s_setprio 1
.Lprio_skip:
	s_lshl_b32 s56, s0, 14
	s_add_i32 s57, s26, s56
	s_add_i32 s58, s0, s4
	s_cmp_gt_u32 s1, 63
	s_cselect_b64 s[82:83], -1, 0
	v_and_b32_e32 v129, 63, v150
	s_and_b64 vcc, exec, s[82:83]
	s_cbranch_vccnz .LBB0_703
	v_lshl_add_u32 v0, v129, 2, s57
	v_or_b32_e32 v1, 64, v129
	ds_write2st64_b32 v0, v129, v1 offset0:48 offset1:49
	v_or_b32_e32 v1, 0x80, v129
	s_waitcnt lgkmcnt(0)
	v_or_b32_e32 v2, 0xc0, v129
	s_add_i32 s16, s58, 1
	s_mov_b64 s[2:3], 0
	ds_write2st64_b32 v0, v1, v2 offset0:50 offset1:51
